# attention main loop: K/V LDS-DMA pieces without m0 save/restore, address temporary and s_nop (m0 written two SALU ops ahead; m0 parked in s32 across the loop)
# speedup vs baseline: 1.0136x; 1.0007x over previous
; #define LAS __attribute__((address_space(3)))
; #define WAIT_BAR(N) asm volatile("s_waitcnt vmcnt(" #N ") lgkmcnt(0)\n\ts_barrier" ::: "memory")
;     __device__ __forceinline__ const float* x() const { return (const float*)ld(0); }
; template <int THRL> ...
;   const int tid = threadIdx.x, lane = tid & 63, r32 = lane & 31, hi = lane >> 5; const int wid = __builtin_amdgcn_readfirstlane(tid >> 6);
;   const int comp = wid >> 2, wq = wid & 3;
;   if (wid >= 4) __builtin_amdgcn_s_setprio(1);
;   const bf16_t* Qw = Q + (size_t)(CTXL + qb * 128 + wq * QBLK) * DMK + head * 128 + comp * 64;
;   const bf16_t* Kh = K + head * 128; const bf16_t* Vh = V + head * 128;
;   const unsigned lds0 = (unsigned)(uintptr_t)shm;
;   LAS float* wsf = (LAS float*)(shm + LDS_WS) + wid * 64;
;   const unsigned kvoff = (unsigned)(lane * DMK + wid * 8) * 2u;
;   const unsigned vvoff = (unsigned)((16 * (wid & 3) + (lane >> 2)) * DMK + (wid >> 2) * 32 + (lane & 3) * 8) * 2u;
;   const unsigned kdst = lds0 + LDS_K + wid * 1024, vdst = lds0 + LDS_V + wid * 1024;
;     ...
;   const int vb0 = (int)(lds0 + LDS_V) + ((lane >> 4) & 1) * 32 + (lane & 3) * 8 + (4 * hi + ((lane & 15) >> 2)) * 64;
;   bf16x8 kf[8];
;   const lds_cptr shm3 = (lds_cptr)shm; const lds_cptr kp0 = shm3 + LDS_K + comp * 8192 + hi * 1024 + r32 * 16;
;   const lds_cptr vp0 = shm3 + LDS_V + ((lane >> 4) & 1) * 32 + (lane & 3) * 8 + (4 * hi + ((lane & 15) >> 2)) * 64;
;   DMA_K(0, 0); DMA_V(0, 0); DMA_K(1, SLOTB);
;   bf16x8 qr[4];
; #pragma unroll
;   for (int d0 = 0; d0 < 4; ++d0) qr[d0] = *reinterpret_cast<const bf16x8*>(&Qw[(long)r32 * DMK + d0 * 16 + hi * 8]);
;   float mhat = 0.f, l_reg = 0.f; f32x16 o[4]; o[0] = f32x16{}; o[1] = f32x16{}; o[2] = f32x16{}; o[3] = f32x16{}; f32x16 negm = f32x16{}; asm volatile("" : "+v"(negm));
;   bool resc = false;
;     ...
;   f32x16 pA0, pA1, pB0, pB1;
;   int sl_prev = 0, sl_cur = 0, sl_next = SLOTB;
;     ...
;   DMA_K(2, 2 * SLOTB);
;   WAIT_BAR(6);
;   qkt(pA0, pA1, kp0, qr, negm); asm volatile("s_nop 15\n\ts_nop 7" : "+v"(pA0), "+v"(pA1));
;   const lds_cptr qp = shm3 + LDS_Q + wid * 4096 + lane * 16;
; #pragma unroll
;   for (int d0 = 0; d0 < 4; ++d0) *(LAS bf16x8*)(shm + LDS_Q + wid * 4096 + lane * 16 + d0 * 1024) = qr[d0];
;   START(pA0, pA1);
.LBB0_527:
	s_lshl_b32 s0, s28, 1
	s_and_b32 s0, s0, 0x700
	s_add_u32 s33, s26, s0
	s_addc_u32 s53, s27, 0
	s_bfe_u32 s41, s39, 0x20006
	s_lshl_b32 s0, s36, 4
	s_and_b32 s37, s0, 0xffffff80
	s_lshl_b32 s0, s41, 5
	s_or_b32 s0, s37, s0
	s_addk_i32 s0, 0x100
	s_ashr_i32 s1, s0, 31
	s_lshr_b32 s40, s39, 6
	s_lshr_b32 s42, s39, 8
	s_lshl_b64 s[0:1], s[0:1], 11
	s_add_u32 s0, s5, s0
	s_addc_u32 s1, s17, s1
	s_lshl_b32 s2, s36, 7
	s_and_b32 s14, s2, 0x380
	s_lshl_b32 s8, s14, 1
	s_add_u32 s0, s0, s8
	s_addc_u32 s1, s1, 0
	s_lshl_b32 s43, s42, 6
	s_lshl_b32 s2, s42, 7
	s_add_u32 s2, s0, s2
	s_addc_u32 s3, s1, 0
	s_add_u32 s20, s22, s8
	s_addc_u32 s21, s23, 0
	s_add_u32 s8, s24, s8
	s_addc_u32 s9, s25, 0
	s_lshl_b32 s0, s41, 15
	s_add_i32 s0, s0, s43
	v_add_u32_e32 v235, s0, v219
	s_lshl_b32 s0, s40, 10
	s_add_i32 s49, s0, 0
	s_and_b32 s1, s39, 0x3fffffc0
	s_lshl_b32 s38, s40, 4
	s_add_i32 s46, s49, 0xc000
	s_add_u32 s44, s20, 0x80
	v_add_u32_e32 v237, s38, v218
	s_mov_b32 s0, m0
	s_mov_b32 m0, s49
	s_nop 0
	global_load_lds_dwordx4 v237, s[20:21] offset:0
	s_mov_b32 m0, s0
	s_addc_u32 s45, s21, 0
	s_add_i32 s54, s49, 0x2000
	s_mov_b32 s0, m0
	s_mov_b32 m0, s54
	s_nop 0
	global_load_lds_dwordx4 v237, s[44:45] offset:0
	s_mov_b32 m0, s0
	s_add_u32 s50, s8, 0x80
	s_mov_b32 s0, m0
	s_mov_b32 m0, s46
	s_nop 0
	global_load_lds_dwordx4 v235, s[8:9] offset:0
	s_mov_b32 m0, s0
	s_addc_u32 s51, s9, 0
	s_add_i32 s45, s49, 0xe000
	s_mov_b32 s0, m0
	s_mov_b32 m0, s45
	s_nop 0
	global_load_lds_dwordx4 v235, s[50:51] offset:0
	s_mov_b32 m0, s0
	s_add_u32 s50, s20, 0x20000
	s_addc_u32 s51, s21, 0
	s_add_i32 s52, s49, 0x4000
	s_mov_b32 s0, m0
	s_mov_b32 m0, s52
	s_nop 0
	global_load_lds_dwordx4 v237, s[50:51] offset:0
	s_mov_b32 m0, s0
	s_add_u32 s56, s20, 0x20080
	s_addc_u32 s57, s21, 0
	s_add_i32 s51, s49, 0x6000
	s_mov_b32 s0, m0
	s_mov_b32 m0, s51
	s_nop 0
	global_load_lds_dwordx4 v237, s[56:57] offset:0
	s_mov_b32 m0, s0
	global_load_dwordx4 v[66:69], v229, s[2:3]
	global_load_dwordx4 v[70:73], v229, s[2:3] offset:32
	global_load_dwordx4 v[74:77], v229, s[2:3] offset:64
	global_load_dwordx4 v[78:81], v229, s[2:3] offset:96
	v_mov_b64_e32 v[48:49], v[32:33]
	s_add_u32 s2, s20, 0x40000
	v_mov_b64_e32 v[46:47], v[30:31]
	v_mov_b64_e32 v[44:45], v[28:29]
	v_mov_b64_e32 v[42:43], v[26:27]
	v_mov_b64_e32 v[40:41], v[24:25]
	v_mov_b64_e32 v[38:39], v[22:23]
	v_mov_b64_e32 v[36:37], v[20:21]
	v_mov_b64_e32 v[34:35], v[18:19]
	s_addc_u32 s3, s21, 0
	s_add_i32 s48, s49, 0x8000
	s_mov_b32 s0, m0
	s_mov_b32 m0, s48
	s_nop 0
	global_load_lds_dwordx4 v237, s[2:3] offset:0
	s_mov_b32 m0, s0
	s_add_u32 s2, s20, 0x40080
	s_addc_u32 s3, s21, 0
	s_add_i32 s47, s49, 0xa000
	s_mov_b32 s0, m0
	s_mov_b32 m0, s47
	s_nop 0
	global_load_lds_dwordx4 v237, s[2:3] offset:0
	s_mov_b32 m0, s0
	v_lshl_add_u32 v236, s42, 13, v221
	s_waitcnt vmcnt(6) lgkmcnt(0)
	s_barrier
	ds_read_b128 v[4:7], v236
	s_lshl_b32 s2, s40, 12
	v_add_u32_e32 v233, s2, v222
	s_lshl_b32 s1, s1, 2
	s_add_i32 s50, s1, 0
	s_add_i32 s50, s50, 0x18000
	s_add_u32 s2, s20, 0x60000
	s_addc_u32 s3, s21, 0
	v_mov_b32_e32 v3, v2
	v_mov_b32_e32 v12, v2
	v_mov_b32_e32 v13, v2
	s_movk_i32 s57, 0x4000
	s_mov_b32 s0, 0
	s_mov_b32 s55, 0x8000
	v_lshl_add_u32 v232, v217, 2, s50
	v_mov_b32_e32 v238, 0
	s_mov_b32 s56, -1
	s_waitcnt vmcnt(3) lgkmcnt(0)
	v_mfma_f32_32x32x16_bf16 v[50:65], v[4:7], v[66:69], v[34:49]
	ds_read_b128 v[4:7], v236 offset:512
	s_waitcnt lgkmcnt(0)
	v_mfma_f32_32x32x16_bf16 v[34:49], v[4:7], v[66:69], v[34:49]
	ds_read_b128 v[4:7], v236 offset:2048
	s_waitcnt vmcnt(2) lgkmcnt(0)
	v_mfma_f32_32x32x16_bf16 v[50:65], v[4:7], v[70:73], v[50:65]
	ds_read_b128 v[4:7], v236 offset:2560
	s_waitcnt lgkmcnt(0)
	v_mfma_f32_32x32x16_bf16 v[34:49], v[4:7], v[70:73], v[34:49]
	ds_read_b128 v[4:7], v236 offset:4096
	ds_read_b128 v[8:11], v236 offset:4608
	ds_read_b128 v[82:85], v236 offset:6656
	ds_read_b128 v[14:17], v236 offset:6144
	s_waitcnt vmcnt(1) lgkmcnt(3)
	v_mfma_f32_32x32x16_bf16 v[50:65], v[4:7], v[74:77], v[50:65]
	v_mov_b32_e32 v4, v2
	v_mov_b32_e32 v5, v2
	v_mov_b32_e32 v6, v2
	v_mov_b32_e32 v7, v2
	s_waitcnt lgkmcnt(2)
	v_mfma_f32_32x32x16_bf16 v[34:49], v[8:11], v[74:77], v[34:49]
	v_mov_b32_e32 v8, v2
	v_mov_b32_e32 v9, v2
	v_mov_b32_e32 v10, v2
	v_mov_b32_e32 v11, v2
	s_waitcnt vmcnt(0) lgkmcnt(0)
	v_mfma_f32_32x32x16_bf16 v[50:65], v[14:17], v[78:81], v[50:65]
	v_mov_b32_e32 v16, v2
	v_mov_b32_e32 v17, v2
	v_mov_b32_e32 v14, v2
	v_mov_b32_e32 v15, v2
	v_mfma_f32_32x32x16_bf16 v[34:49], v[82:85], v[78:81], v[34:49]
	s_nop 15
	s_nop 7
	ds_write_b128 v233, v[66:69]
	ds_write_b128 v233, v[70:73] offset:1024
	ds_write_b128 v233, v[74:77] offset:2048
	ds_write_b128 v233, v[78:81] offset:3072
	v_max3_f32 v66, v50, v51, v34
	v_max3_f32 v67, v52, v53, v35
	v_mov_b64_e32 v[96:97], v[16:17]
	v_max3_f32 v66, v66, v36, v37
	v_max3_f32 v67, v67, v56, v57
	v_mov_b64_e32 v[94:95], v[14:15]
	v_max3_f32 v66, v66, v54, v55
	v_max3_f32 v67, v67, v40, v41
	v_mov_b64_e32 v[92:93], v[12:13]
	v_max3_f32 v66, v66, v38, v39
	v_max3_f32 v67, v67, v60, v61
	v_mov_b64_e32 v[90:91], v[10:11]
	v_max3_f32 v66, v66, v58, v59
	v_max3_f32 v67, v67, v44, v45
	v_mov_b64_e32 v[88:89], v[8:9]
	v_max3_f32 v66, v66, v42, v43
	v_max3_f32 v67, v67, v64, v65
	v_mov_b64_e32 v[86:87], v[6:7]
	v_max3_f32 v66, v66, v62, v63
	v_max3_f32 v67, v67, v48, v49
	v_mov_b64_e32 v[84:85], v[4:5]
	v_max3_f32 v66, v66, v46, v47
	v_mov_b64_e32 v[82:83], v[2:3]
	v_max_f32_e32 v66, v66, v67
	s_nop 0
	v_mov_b32_e32 v67, v66
	s_nop 1
	v_permlane32_swap_b32_e32 v66, v67
	v_max_f32_e32 v66, v66, v67
	s_nop 0
	v_add_f32_e32 v234, v2, v66
	v_sub_f32_e32 v50, v50, v66
	v_sub_f32_e32 v34, v34, v66
	v_sub_f32_e32 v51, v51, v66
	v_sub_f32_e32 v35, v35, v66
	v_sub_f32_e32 v52, v52, v66
	s_nop 0
	v_xor_b32_e32 v98, 0x80000000, v234
	v_mov_b32_e32 v99, v98
	v_mov_b32_e32 v100, v98
	v_mov_b32_e32 v101, v98
	v_mov_b32_e32 v102, v98
	v_mov_b32_e32 v103, v98
	v_mov_b32_e32 v104, v98
	v_mov_b32_e32 v105, v98
	v_mov_b32_e32 v106, v98
	v_mov_b32_e32 v107, v98
	v_mov_b32_e32 v108, v98
	v_mov_b32_e32 v109, v98
	v_mov_b32_e32 v110, v98
	v_mov_b32_e32 v111, v98
	v_mov_b32_e32 v112, v98
	v_mov_b32_e32 v113, v98
	s_waitcnt vmcnt(0) lgkmcnt(0)
	s_barrier
; #define LAS __attribute__((address_space(3)))
; #define WAIT_BAR(N) asm volatile("s_waitcnt vmcnt(" #N ") lgkmcnt(0)\n\ts_barrier" ::: "memory")
; #define DMA_K(t, slot) do { const bf16_t* sb_ = Kh + (long)(t) * KVBLK * DMK; glds16<0>(sb_, kvoff, (unsigned)__builtin_amdgcn_readfirstlane(kdst + (slot))); glds16<0>(sb_ + 64, kvoff, (unsigned)__builtin_amdgcn_readfirstlane(kdst + 8192 + (slot))); } while (0)
; #define DMA_V(t, slot) do { const bf16_t* sb_ = Vh + (long)(t) * KVBLK * DMK; glds16<0>(sb_, vvoff, (unsigned)__builtin_amdgcn_readfirstlane(vdst + (slot))); glds16<0>(sb_ + 64, vvoff, (unsigned)__builtin_amdgcn_readfirstlane(vdst + 8192 + (slot))); } while (0)
; #define ROT() do { sl_prev = sl_cur; sl_cur = sl_next; sl_next = (sl_next == (NSLOT - 1) * SLOTB) ? 0 : sl_next + SLOTB; } while (0)
;     __device__ __forceinline__ const float* w_gate() const { return (const float*)ld(21); }
; template <int THRL> ...
;     ...
;   START(pA0, pA1);
; #pragma unroll
;   for (int r = 0; r < 16; ++r) pA1[r] = __builtin_amdgcn_exp2f(pA1[r]);
;   WAIT_BAR(0);
;   DMA_K(3, 0); DMA_V(1, SLOTB);
;   ROT();
;   kload8(kf, kp0 + sl_cur);
;   WAIT_BAR(4);
; __device__ __forceinline__ void convert_moe_items(const Ctx& a, int layer, LAS unsigned char* lds, int it0, int it1, int widx, int nw, int wave, int lane) {
;     LAS float* scr = (LAS float*)(lds + wave * 16384);
;     bf16_t* WGU = (bf16_t*)(a.ws() + WS_WGU + (size_t)layer * WGU_BYTES); bf16_t* WD = (bf16_t*)(a.ws() + WS_WD + (size_t)layer * WD_BYTES);
;     constexpr int I_G = (DM / 64) * (FE / 32), I_D = (FE / 64) * (DM / 32);
;     constexpr int PER_E = 2 * I_G + I_D;
;     const float *wg = a.w_gate(), *wu = a.w_up(), *wd = a.w_down();
;     auto decode = [&](int it) { CvtItem d; const int e = it / PER_E; int r = it % PER_E; const size_t eo = ((size_t)layer * NE + e) * (size_t)DM * FE;
;         if (r < I_G)          { d.src = wg + eo; d.dst = WGU; d.N = FE; d.K = DM; d.row_off = e * 2048; d.ilv = 1; }
;         else if (r < 2 * I_G) { r -= I_G; d.src = wu + eo; d.dst = WGU; d.N = FE; d.K = DM; d.row_off = e * 2048 + 128; d.ilv = 1; }
;         else                  { r -= 2 * I_G; d.src = wd + eo; d.dst = WD; d.N = DM; d.K = FE; d.row_off = e * 2048; d.ilv = 0; }
;         const int nblk = d.N / 32; d.k0 = 64 * (r / nblk); d.n0 = 32 * (r % nblk); return d; };
;     int it = it0 + widx;
	s_mov_b32 s1, m0
	s_mov_b32 m0, s49
	s_nop 0
	global_load_lds_dwordx4 v237, s[2:3] offset:0
	s_mov_b32 m0, s1
	s_add_u32 s2, s20, 0x60080
	s_addc_u32 s3, s21, 0
	s_mov_b32 s1, m0
	s_mov_b32 m0, s54
	s_nop 0
	global_load_lds_dwordx4 v237, s[2:3] offset:0
	s_mov_b32 m0, s1
	s_add_u32 s2, s8, 0x20000
	s_addc_u32 s3, s9, 0
	s_add_i32 s44, s49, 0x10000
	s_mov_b32 s1, m0
	s_mov_b32 m0, s44
	s_nop 0
	global_load_lds_dwordx4 v235, s[2:3] offset:0
	s_mov_b32 m0, s1
	s_add_u32 s2, s8, 0x20080
	s_addc_u32 s3, s9, 0
	s_add_i32 s43, s49, 0x12000
	s_mov_b32 s1, m0
	s_mov_b32 m0, s43
	s_nop 0
	global_load_lds_dwordx4 v235, s[2:3] offset:0
	s_mov_b32 m0, s1
	ds_read_b128 v[146:149], v236 offset:16384
	ds_read_b128 v[202:205], v236 offset:16896
	ds_read_b128 v[206:209], v236 offset:18432
	ds_read_b128 v[190:193], v236 offset:18944
	ds_read_b128 v[198:201], v236 offset:20480
	ds_read_b128 v[186:189], v236 offset:20992
	ds_read_b128 v[182:185], v236 offset:22528
	ds_read_b128 v[178:181], v236 offset:23040
	v_sub_f32_e32 v36, v36, v66
	v_sub_f32_e32 v53, v53, v66
	v_sub_f32_e32 v37, v37, v66
	v_sub_f32_e32 v54, v54, v66
	v_sub_f32_e32 v38, v38, v66
	v_sub_f32_e32 v55, v55, v66
	v_sub_f32_e32 v39, v39, v66
	v_sub_f32_e32 v56, v56, v66
	v_sub_f32_e32 v40, v40, v66
	v_sub_f32_e32 v57, v57, v66
	v_sub_f32_e32 v41, v41, v66
	v_sub_f32_e32 v58, v58, v66
	v_sub_f32_e32 v42, v42, v66
	v_sub_f32_e32 v59, v59, v66
	v_sub_f32_e32 v43, v43, v66
	v_sub_f32_e32 v60, v60, v66
	v_sub_f32_e32 v44, v44, v66
	v_sub_f32_e32 v61, v61, v66
	v_sub_f32_e32 v45, v45, v66
	v_sub_f32_e32 v62, v62, v66
	v_sub_f32_e32 v46, v46, v66
	v_sub_f32_e32 v63, v63, v66
	v_sub_f32_e32 v47, v47, v66
	v_sub_f32_e32 v64, v64, v66
	v_sub_f32_e32 v48, v48, v66
	v_sub_f32_e32 v65, v65, v66
	v_sub_f32_e32 v49, v49, v66
	v_exp_f32_e32 v130, v50
	v_exp_f32_e32 v131, v51
	v_exp_f32_e32 v132, v52
	v_exp_f32_e32 v133, v53
	v_exp_f32_e32 v134, v54
	v_exp_f32_e32 v135, v55
	v_exp_f32_e32 v136, v56
	v_exp_f32_e32 v137, v57
	v_exp_f32_e32 v138, v58
	v_exp_f32_e32 v139, v59
	v_exp_f32_e32 v140, v60
	v_exp_f32_e32 v141, v61
	v_exp_f32_e32 v142, v62
	v_exp_f32_e32 v143, v63
	v_exp_f32_e32 v144, v64
	v_exp_f32_e32 v145, v65
	v_exp_f32_e32 v114, v34
	v_exp_f32_e32 v115, v35
	v_exp_f32_e32 v116, v36
	v_exp_f32_e32 v117, v37
	v_exp_f32_e32 v118, v38
	v_exp_f32_e32 v119, v39
	v_exp_f32_e32 v120, v40
	v_exp_f32_e32 v121, v41
	v_exp_f32_e32 v122, v42
	v_exp_f32_e32 v123, v43
	v_exp_f32_e32 v124, v44
	v_exp_f32_e32 v125, v45
	v_exp_f32_e32 v126, v46
	v_exp_f32_e32 v127, v47
	v_exp_f32_e32 v128, v48
	v_exp_f32_e32 v129, v49
	s_waitcnt vmcnt(4) lgkmcnt(0)
	s_barrier
	v_mov_b64_e32 v[80:81], v[16:17]
	v_mov_b64_e32 v[48:49], v[16:17]
	v_mov_b64_e32 v[64:65], v[16:17]
	v_mov_b64_e32 v[78:79], v[14:15]
	v_mov_b64_e32 v[76:77], v[12:13]
	v_mov_b64_e32 v[74:75], v[10:11]
	v_mov_b64_e32 v[72:73], v[8:9]
	v_mov_b64_e32 v[70:71], v[6:7]
	v_mov_b64_e32 v[68:69], v[4:5]
	v_mov_b64_e32 v[66:67], v[2:3]
	v_mov_b64_e32 v[46:47], v[14:15]
	v_mov_b64_e32 v[44:45], v[12:13]
	v_mov_b64_e32 v[42:43], v[10:11]
	v_mov_b64_e32 v[40:41], v[8:9]
	v_mov_b64_e32 v[38:39], v[6:7]
	v_mov_b64_e32 v[36:37], v[4:5]
	v_mov_b64_e32 v[34:35], v[2:3]
	v_mov_b64_e32 v[62:63], v[14:15]
	v_mov_b64_e32 v[60:61], v[12:13]
	v_mov_b64_e32 v[58:59], v[10:11]
	v_mov_b64_e32 v[56:57], v[8:9]
	v_mov_b64_e32 v[54:55], v[6:7]
	v_mov_b64_e32 v[52:53], v[4:5]
	v_mov_b64_e32 v[50:51], v[2:3]
	v_mov_b32_e32 v244, 0x23ee8
	ds_read2_b64 v[250:253], v244 offset1:1
	ds_read_b64 v[254:255], v244 offset:16
	s_waitcnt lgkmcnt(0)
	v_readfirstlane_b32 s68, v250
	v_readfirstlane_b32 s69, v251
	v_readfirstlane_b32 s70, v252
	v_readfirstlane_b32 s71, v253
	v_readfirstlane_b32 s72, v254
	v_readfirstlane_b32 s73, v255
	ds_read_b64 v[250:251], v244 offset:40
	s_waitcnt lgkmcnt(0)
	v_readfirstlane_b32 s74, v250
	v_readfirstlane_b32 s75, v251
	s_add_u32 s76, s74, 0x16530000
	s_addc_u32 s77, s75, 0
	s_add_u32 s74, s74, 0xa530000
	s_addc_u32 s75, s75, 0
	v_lshrrev_b32_e32 v25, 3, v214
	v_and_b32_e32 v28, 7, v214
	v_lshlrev_b32_e32 v33, 4, v28
	v_lshl_add_u32 v24, v25, 12, v33
	v_lshl_add_u32 v246, v25, 13, v33
	v_lshlrev_b32_e32 v29, 8, v28
	v_lshl_add_u32 v29, v25, 1, v29
	s_lshl_b32 s2, s40, 11
	s_cmp_lt_u32 s40, 6
	s_mov_b32 s3, 0x21000
	s_cselect_b32 s3, 0x20800, s3
	s_add_i32 s2, s2, s3
	v_add_u32_e32 v29, s2, v29
	v_add_u32_e32 v29, 32, v29
	v_lshl_add_u32 v32, v214, 3, s2
	s_mul_i32 s66, s96, 8
	s_add_i32 s66, s66, s40
	s_cmpk_lt_u32 s36, 0x100
	s_movk_i32 s67, 104
	s_cselect_b32 s67, 104, s67
	s_cselect_b32 s2, 0, 0x6800
	s_add_i32 s66, s66, s2
	s_add_i32 s90, s67, 6
	s_cmp_eq_u32 s67, 0
	s_cselect_b32 s90, -1, s90
	global_load_dword v249, v24, s[68:69]
	global_load_dword v249, v24, s[68:69]
	s_mov_b32 s32, m0

.LBB0_529:
	v_mfma_f32_32x32x16_bf16 v[66:81], v[194:197], v[134:137], v[66:81]
	v_exp_f32_e32 v162, v162
	v_exp_f32_e32 v163, v163
	ds_read_b64_tr_b16 v[122:123], v16 offset:50176
	ds_read_b64_tr_b16 v[124:125], v16 offset:50688
	s_add_u32 s58, s33, 0xfef80000
	s_addc_u32 s59, s53, -1
	s_add_i32 m0, s57, s49
	s_add_u32 s2, s33, 0xfefe0000
	s_addc_u32 s3, s53, -1
	global_load_lds_dwordx4 v237, s[2:3] offset:0
	v_mfma_f32_32x32x16_bf16 v[82:97], v[194:197], v[130:133], v[82:97]
	v_exp_f32_e32 v164, v164
	v_exp_f32_e32 v165, v165
	ds_read_b64_tr_b16 v[126:127], v16 offset:54272
	ds_read_b64_tr_b16 v[128:129], v16 offset:54784
	s_waitcnt lgkmcnt(6)
	v_mfma_f32_32x32x16_bf16 v[34:49], v[194:197], v[118:121], v[34:49]
	v_exp_f32_e32 v166, v166
	v_exp_f32_e32 v167, v167
	ds_read_b64_tr_b16 v[130:131], v16 offset:58368
	ds_read_b64_tr_b16 v[132:133], v16 offset:58880
	s_add_i32 m0, s57, s54
	s_add_u32 s2, s33, 0xfefe0080
	s_addc_u32 s3, s53, -1
	global_load_lds_dwordx4 v237, s[2:3] offset:0
	s_waitcnt lgkmcnt(6)
	v_mfma_f32_32x32x16_bf16 v[50:65], v[194:197], v[114:117], v[50:65]
	v_exp_f32_e32 v168, v168
	v_exp_f32_e32 v169, v169
	ds_read_b64_tr_b16 v[118:119], v16 offset:62464
	ds_read_b64_tr_b16 v[120:121], v16 offset:62976
	v_add_u32_e32 v17, s55, v236
	ds_read_b128 v[114:117], v17
	ds_read_b128 v[178:181], v17 offset:512
	s_waitcnt lgkmcnt(8)
	v_mfma_f32_32x32x16_bf16 v[66:81], v[12:15], v[122:125], v[66:81]
	v_exp_f32_e32 v170, v170
	v_exp_f32_e32 v171, v171
	ds_read_b64_tr_b16 v[134:135], v16 offset:51200
	ds_read_b64_tr_b16 v[136:137], v16 offset:51712
	s_add_i32 m0, s55, s46
	s_add_u32 s2, s33, 0x20000
	s_addc_u32 s3, s53, 0
	global_load_lds_dwordx4 v235, s[2:3] offset:0
	s_waitcnt lgkmcnt(8)
	v_mfma_f32_32x32x16_bf16 v[82:97], v[12:15], v[126:129], v[82:97]
	v_exp_f32_e32 v172, v172
	v_exp_f32_e32 v173, v173
	ds_read_b64_tr_b16 v[122:123], v16 offset:55296
	ds_read_b64_tr_b16 v[124:125], v16 offset:55808
	ds_read_b128 v[198:201], v17 offset:2048
	ds_read_b128 v[186:189], v17 offset:2560
	s_waitcnt lgkmcnt(10)
	v_mfma_f32_32x32x16_bf16 v[34:49], v[12:15], v[130:133], v[34:49]
	v_exp_f32_e32 v174, v174
	v_exp_f32_e32 v175, v175
	ds_read_b64_tr_b16 v[126:127], v16 offset:59392
	ds_read_b64_tr_b16 v[128:129], v16 offset:59904
	s_add_i32 m0, s55, s45
	s_add_u32 s2, s33, 0x20080
	s_addc_u32 s3, s53, 0
	global_load_lds_dwordx4 v235, s[2:3] offset:0
	s_waitcnt lgkmcnt(10)
	v_mfma_f32_32x32x16_bf16 v[50:65], v[12:15], v[118:121], v[50:65]
	v_exp_f32_e32 v176, v176
	v_exp_f32_e32 v177, v177
	ds_read_b64_tr_b16 v[130:131], v16 offset:63488
	ds_read_b64_tr_b16 v[132:133], v16 offset:64000
	ds_read_b128 v[206:209], v17 offset:4096
	ds_read_b128 v[190:193], v17 offset:4608
	s_waitcnt lgkmcnt(10)
	v_mfma_f32_32x32x16_bf16 v[66:81], v[8:11], v[134:137], v[66:81]
	v_exp_f32_e32 v146, v146
	v_exp_f32_e32 v147, v147
	ds_read_b64_tr_b16 v[118:119], v16 offset:52224
	ds_read_b64_tr_b16 v[120:121], v16 offset:52736
	s_waitcnt lgkmcnt(10)
	v_mfma_f32_32x32x16_bf16 v[82:97], v[8:11], v[122:125], v[82:97]
	v_exp_f32_e32 v148, v148
	v_exp_f32_e32 v149, v149
	ds_read_b64_tr_b16 v[134:135], v16 offset:56320
	ds_read_b64_tr_b16 v[136:137], v16 offset:56832
	ds_read_b128 v[202:205], v17 offset:6144
	ds_read_b128 v[182:185], v17 offset:6656
	s_waitcnt lgkmcnt(10)
	v_mfma_f32_32x32x16_bf16 v[34:49], v[8:11], v[126:129], v[34:49]
	v_exp_f32_e32 v150, v150
	v_exp_f32_e32 v151, v151
	ds_read_b64_tr_b16 v[122:123], v16 offset:60416
	ds_read_b64_tr_b16 v[124:125], v16 offset:60928
	s_waitcnt lgkmcnt(10)
	v_mfma_f32_32x32x16_bf16 v[50:65], v[8:11], v[130:133], v[50:65]
	v_exp_f32_e32 v152, v152
	v_exp_f32_e32 v153, v153
	ds_read_b64_tr_b16 v[126:127], v16 offset:64512
	ds_read_b64_tr_b16 v[128:129], v16 offset:65024
	s_waitcnt lgkmcnt(8)
	v_mfma_f32_32x32x16_bf16 v[66:81], v[4:7], v[118:121], v[66:81]
	v_exp_f32_e32 v154, v154
	v_exp_f32_e32 v155, v155
	s_waitcnt lgkmcnt(6)
	v_mfma_f32_32x32x16_bf16 v[82:97], v[4:7], v[134:137], v[82:97]
	v_exp_f32_e32 v156, v156
	v_exp_f32_e32 v157, v157
	s_waitcnt lgkmcnt(2)
	v_mfma_f32_32x32x16_bf16 v[34:49], v[4:7], v[122:125], v[34:49]
	v_exp_f32_e32 v158, v158
	v_exp_f32_e32 v159, v159
	s_add_i32 s2, s56, 1
	s_cmp_gt_i32 s2, s90
	s_cbranch_scc1 .Lcs_done_h0
	s_waitcnt vmcnt(6)
	v_cvt_pk_bf16_f32 v245, v250, v251
	v_cvt_pk_bf16_f32 v244, v252, v253
	s_cmp_lt_u32 s2, 7
	s_cbranch_scc1 .Lcs_dumS_h0
	s_bitcmp1_b32 s2, 1
	s_cbranch_scc1 .Lcs_Sb_h0
	global_store_dwordx2 v28, v[30:31], s[100:101] nt
	v_add_u32_e32 v28, s63, v28

.LBB0_532:
	s_add_i32 s2, s55, 0x4000
	s_cmpk_lg_u32 s55, 0x8000
	s_cselect_b32 s57, s2, 0
	v_mfma_f32_32x32x16_bf16 v[66:81], v[194:197], v[166:169], v[66:81]
	v_exp_f32_e32 v130, v130
	v_exp_f32_e32 v131, v131
	ds_read_b64_tr_b16 v[154:155], v16 offset:50176
	ds_read_b64_tr_b16 v[156:157], v16 offset:50688
	s_add_i32 m0, s55, s49
	s_add_u32 s2, s58, 0x80000
	s_addc_u32 s3, s59, 0
	global_load_lds_dwordx4 v237, s[2:3] offset:0
	v_mfma_f32_32x32x16_bf16 v[82:97], v[194:197], v[162:165], v[82:97]
	v_exp_f32_e32 v132, v132
	v_exp_f32_e32 v133, v133
	ds_read_b64_tr_b16 v[158:159], v16 offset:54272
	ds_read_b64_tr_b16 v[160:161], v16 offset:54784
	s_waitcnt lgkmcnt(6)
	v_mfma_f32_32x32x16_bf16 v[34:49], v[194:197], v[150:153], v[34:49]
	v_exp_f32_e32 v134, v134
	v_exp_f32_e32 v135, v135
	ds_read_b64_tr_b16 v[162:163], v16 offset:58368
	ds_read_b64_tr_b16 v[164:165], v16 offset:58880
	s_add_i32 m0, s55, s54
	s_add_u32 s2, s58, 0x80080
	s_addc_u32 s3, s59, 0
	global_load_lds_dwordx4 v237, s[2:3] offset:0
	s_waitcnt lgkmcnt(6)
	v_mfma_f32_32x32x16_bf16 v[50:65], v[194:197], v[146:149], v[50:65]
	v_exp_f32_e32 v136, v136
	v_exp_f32_e32 v137, v137
	ds_read_b64_tr_b16 v[150:151], v16 offset:62464
	ds_read_b64_tr_b16 v[152:153], v16 offset:62976
	v_add_u32_e32 v3, s57, v236
	ds_read_b128 v[146:149], v3
	ds_read_b128 v[202:205], v3 offset:512
	s_waitcnt lgkmcnt(8)
	v_mfma_f32_32x32x16_bf16 v[66:81], v[12:15], v[154:157], v[66:81]
	v_exp_f32_e32 v138, v138
	v_exp_f32_e32 v139, v139
	ds_read_b64_tr_b16 v[166:167], v16 offset:51200
	ds_read_b64_tr_b16 v[168:169], v16 offset:51712
	s_add_i32 m0, s57, s46
	s_add_u32 s2, s33, 0x40000
	s_addc_u32 s3, s53, 0
	global_load_lds_dwordx4 v235, s[2:3] offset:0
	s_waitcnt lgkmcnt(8)
	v_mfma_f32_32x32x16_bf16 v[82:97], v[12:15], v[158:161], v[82:97]
	v_exp_f32_e32 v140, v140
	v_exp_f32_e32 v141, v141
	ds_read_b64_tr_b16 v[154:155], v16 offset:55296
	ds_read_b64_tr_b16 v[156:157], v16 offset:55808
	ds_read_b128 v[206:209], v3 offset:2048
	ds_read_b128 v[190:193], v3 offset:2560
	s_waitcnt lgkmcnt(10)
	v_mfma_f32_32x32x16_bf16 v[34:49], v[12:15], v[162:165], v[34:49]
	v_exp_f32_e32 v142, v142
	v_exp_f32_e32 v143, v143
	ds_read_b64_tr_b16 v[158:159], v16 offset:59392
	ds_read_b64_tr_b16 v[160:161], v16 offset:59904
	s_add_i32 m0, s57, s45
	s_add_u32 s2, s33, 0x40080
	s_addc_u32 s3, s53, 0
	global_load_lds_dwordx4 v235, s[2:3] offset:0
	s_waitcnt lgkmcnt(10)
	v_mfma_f32_32x32x16_bf16 v[50:65], v[12:15], v[150:153], v[50:65]
	v_exp_f32_e32 v144, v144
	v_exp_f32_e32 v145, v145
	ds_read_b64_tr_b16 v[162:163], v16 offset:63488
	ds_read_b64_tr_b16 v[164:165], v16 offset:64000
	ds_read_b128 v[198:201], v3 offset:4096
	ds_read_b128 v[186:189], v3 offset:4608
	s_waitcnt lgkmcnt(10)
	v_mfma_f32_32x32x16_bf16 v[66:81], v[8:11], v[166:169], v[66:81]
	v_exp_f32_e32 v114, v114
	v_exp_f32_e32 v115, v115
	ds_read_b64_tr_b16 v[150:151], v16 offset:52224
	ds_read_b64_tr_b16 v[152:153], v16 offset:52736
	s_waitcnt lgkmcnt(10)
	v_mfma_f32_32x32x16_bf16 v[82:97], v[8:11], v[154:157], v[82:97]
	v_exp_f32_e32 v116, v116
	v_exp_f32_e32 v117, v117
	ds_read_b64_tr_b16 v[166:167], v16 offset:56320
	ds_read_b64_tr_b16 v[168:169], v16 offset:56832
	ds_read_b128 v[182:185], v3 offset:6144
	ds_read_b128 v[178:181], v3 offset:6656
	s_waitcnt lgkmcnt(10)
	v_mfma_f32_32x32x16_bf16 v[34:49], v[8:11], v[158:161], v[34:49]
	v_exp_f32_e32 v118, v118
	v_exp_f32_e32 v119, v119
	ds_read_b64_tr_b16 v[154:155], v16 offset:60416
	ds_read_b64_tr_b16 v[156:157], v16 offset:60928
	s_waitcnt lgkmcnt(10)
	v_mfma_f32_32x32x16_bf16 v[50:65], v[8:11], v[162:165], v[50:65]
	v_exp_f32_e32 v120, v120
	v_exp_f32_e32 v121, v121
	ds_read_b64_tr_b16 v[158:159], v16 offset:64512
	ds_read_b64_tr_b16 v[160:161], v16 offset:65024
	s_waitcnt lgkmcnt(8)
	v_mfma_f32_32x32x16_bf16 v[66:81], v[4:7], v[150:153], v[66:81]
	v_exp_f32_e32 v122, v122
	v_exp_f32_e32 v123, v123
	s_waitcnt lgkmcnt(6)
	v_mfma_f32_32x32x16_bf16 v[82:97], v[4:7], v[166:169], v[82:97]
	v_exp_f32_e32 v124, v124
	v_exp_f32_e32 v125, v125
	s_waitcnt lgkmcnt(2)
	v_mfma_f32_32x32x16_bf16 v[34:49], v[4:7], v[154:157], v[34:49]
	v_exp_f32_e32 v126, v126
	v_exp_f32_e32 v127, v127
	s_add_i32 s2, s56, 2
	s_cmp_gt_i32 s2, s90
	s_cbranch_scc1 .Lcs_done_h1
	s_waitcnt vmcnt(6)
	v_cvt_pk_bf16_f32 v245, v18, v19
	v_cvt_pk_bf16_f32 v244, v20, v21
	s_cmp_lt_u32 s2, 7
	s_cbranch_scc1 .Lcs_dumS_h1
	s_and_b32 s61, s2, 7
	s_cmp_eq_u32 s61, 7
	s_cbranch_scc1 .Lcs_adopt_h1

.LBB0_542:
	v_mov_b32_e32 v18, 0
	v_mov_b32_e32 v19, 0
	v_mov_b32_e32 v20, 0
	v_mov_b32_e32 v21, 0
	v_mov_b32_e32 v22, 0
	v_mov_b32_e32 v23, 0
	v_mov_b32_e32 v24, 0
	v_mov_b32_e32 v25, 0
	v_mov_b32_e32 v26, 0
	v_mov_b32_e32 v27, 0
	v_mov_b32_e32 v28, 0
	v_mov_b32_e32 v29, 0
	v_mov_b32_e32 v30, 0
	v_mov_b32_e32 v31, 0
	v_mov_b32_e32 v32, 0
	v_mov_b32_e32 v33, 0
	s_mov_b32 m0, s32
	ds_read_b128 v[240:243], v233
	v_add_f32_e32 v3, v130, v131
	v_add_f32_e32 v3, v132, v3
	v_add_f32_e32 v3, v133, v3
	v_add_f32_e32 v3, v134, v3
	s_waitcnt lgkmcnt(0)
	v_mfma_f32_32x32x16_bf16 v[162:177], v[146:149], v[240:243], v[98:113]
	v_add_f32_e32 v3, v135, v3
	v_cvt_pk_bf16_f32 v194, v130, v131
	v_cvt_pk_bf16_f32 v195, v132, v133
	v_mfma_f32_32x32x16_bf16 v[146:161], v[202:205], v[240:243], v[98:113]
	v_add_f32_e32 v3, v136, v3
	v_add_f32_e32 v3, v137, v3
	v_add_f32_e32 v3, v138, v3
	v_add_f32_e32 v3, v139, v3
	v_cvt_pk_bf16_f32 v196, v134, v135
	v_cvt_pk_bf16_f32 v197, v136, v137
	ds_read_b128 v[130:133], v233 offset:1024
	v_add_f32_e32 v3, v140, v3
	v_add_f32_e32 v3, v141, v3
	v_add_f32_e32 v3, v142, v3
	v_add_f32_e32 v3, v143, v3
	s_waitcnt lgkmcnt(0)
	v_mfma_f32_32x32x16_bf16 v[162:177], v[206:209], v[130:133], v[162:177]
	v_cvt_pk_bf16_f32 v12, v138, v139
	v_cvt_pk_bf16_f32 v13, v140, v141
	v_mfma_f32_32x32x16_bf16 v[146:161], v[190:193], v[130:133], v[146:161]
	v_add_f32_e32 v3, v144, v3
	v_add_f32_e32 v3, v145, v3
	v_add_f32_e32 v3, v114, v3
	v_add_f32_e32 v3, v115, v3
	v_cvt_pk_bf16_f32 v14, v142, v143
	v_cvt_pk_bf16_f32 v15, v144, v145
	ds_read_b128 v[138:141], v233 offset:2048
	ds_read_b64_tr_b16 v[134:135], v223 offset:49152
	ds_read_b64_tr_b16 v[136:137], v223 offset:49664
	s_waitcnt lgkmcnt(2)
	v_mfma_f32_32x32x16_bf16 v[162:177], v[198:201], v[138:141], v[162:177]
	v_add_f32_e32 v3, v116, v3
	v_add_f32_e32 v3, v117, v3
	v_add_f32_e32 v3, v118, v3
	v_add_f32_e32 v3, v119, v3
	v_cvt_pk_bf16_f32 v8, v114, v115
	v_cvt_pk_bf16_f32 v9, v116, v117
	ds_read_b64_tr_b16 v[130:131], v223 offset:53248
	ds_read_b64_tr_b16 v[132:133], v223 offset:53760
	v_mfma_f32_32x32x16_bf16 v[146:161], v[186:189], v[138:141], v[146:161]
	v_add_f32_e32 v3, v120, v3
	v_add_f32_e32 v3, v121, v3
	v_add_f32_e32 v3, v122, v3
	v_add_f32_e32 v3, v123, v3
	v_cvt_pk_bf16_f32 v10, v118, v119
	v_cvt_pk_bf16_f32 v11, v120, v121
	ds_read_b128 v[138:141], v233 offset:3072
	ds_read_b64_tr_b16 v[118:119], v223 offset:57344
	ds_read_b64_tr_b16 v[120:121], v223 offset:57856
	s_waitcnt lgkmcnt(2)
	v_mfma_f32_32x32x16_bf16 v[162:177], v[182:185], v[138:141], v[162:177]
	v_add_f32_e32 v3, v124, v3
	v_add_f32_e32 v3, v125, v3
	v_add_f32_e32 v3, v126, v3
	v_add_f32_e32 v3, v127, v3
	v_cvt_pk_bf16_f32 v4, v122, v123
	v_cvt_pk_bf16_f32 v5, v124, v125
	ds_read_b64_tr_b16 v[114:115], v223 offset:61440
	ds_read_b64_tr_b16 v[116:117], v223 offset:61952
	v_mfma_f32_32x32x16_bf16 v[146:161], v[178:181], v[138:141], v[146:161]
	v_add_f32_e32 v3, v128, v3
	v_add_f32_e32 v3, v129, v3
	v_add_f32_e32 v3, 0, v3
	v_cvt_pk_bf16_f32 v6, v126, v127
	v_cvt_pk_bf16_f32 v7, v128, v129
	v_max_f32_e32 v16, v163, v163
	v_max_f32_e32 v17, v162, v162
	v_max_f32_e32 v16, v17, v16
	s_nop 3
	v_max3_f32 v17, v164, v165, v147
	v_max3_f32 v16, v16, v146, v148
	v_max3_f32 v16, v16, v149, v166
	v_max3_f32 v17, v17, v168, v169
	v_max3_f32 v16, v16, v167, v150
	v_max3_f32 v17, v17, v152, v153
	v_max3_f32 v16, v16, v151, v170
	v_max3_f32 v17, v17, v172, v173
	v_max3_f32 v16, v16, v171, v154
	v_max3_f32 v17, v17, v156, v157
	v_max3_f32 v16, v16, v155, v174
	v_max3_f32 v17, v17, v176, v177
	v_max3_f32 v122, v16, v175, v158
	v_max3_f32 v17, v17, v160, v161
	v_add_f32_e32 v16, v238, v3
	v_max3_f32 v3, v122, v159, v17
	v_mov_b32_e32 v17, v3
	s_nop 1
	v_permlane32_swap_b32_e32 v3, v17
	v_max_f32_e32 v17, v17, v17
	v_max_f32_e32 v3, v3, v3
	v_max_f32_e32 v3, v3, v17
	v_cmp_lt_f32_e32 vcc, s30, v3
	s_cmp_lg_u64 vcc, 0
	s_cselect_b64 s[0:1], -1, 0
	s_cbranch_vccnz .LBB0_565
